# speedup vs baseline: 1.0794x; 1.0083x over previous
.LBB3_36:
	s_andn2_b64 vcc, exec, s[6:7]
	s_cbranch_vccnz .LBB3_86
	s_cmpk_gt_u32 s2, 0xff
	s_cbranch_scc1 .LBB3_86
	s_mov_b64 s[40:41], s[0:1]
	s_mov_b32 s44, s18
	s_mov_b32 s45, s19
	s_mov_b32 s46, 0
	s_mov_b32 s60, s2
	s_mov_b32 s61, 0
	s_mov_b32 s49, 0
	s_mov_b32 s47, 0
	s_mov_b32 s48, 0
	s_movk_i32 s50, 0x63
	s_load_dwordx2 s[52:53], s[0:1], 0x30
	s_add_i32 s51, s19, 31
	s_lshr_b32 s51, s51, 5
	s_sub_i32 s51, s51, 0x200
	s_sub_i32 s55, s51, 1
	s_cmp_lt_u32 s55, 0x80
	s_cselect_b32 s51, s51, 0
	v_mov_b32_e32 v248, v0

.LBB3_57:
	s_or_b64 exec, exec, s[4:5]
	s_movk_i32 s4, 0x619
	v_mul_u32_u24_sdwa v3, v0, s4 dst_sel:DWORD dst_unused:UNUSED_PAD src0_sel:WORD_0 src1_sel:DWORD
	v_lshrrev_b32_e32 v3, 16, v3
	v_mul_lo_u16_e32 v4, 42, v3
	v_sub_u16_e32 v6, v0, v4
	s_movk_i32 s4, 0x64
	v_mov_b32_e32 v4, 0x25600
	v_add_u32_e32 v4, s48, v4
	v_mad_u32_u24 v5, v3, s4, v4
	v_mul_u32_u24_e32 v7, 0x619, v51
	v_min_u32_e32 v19, 0x53f, v56
	s_waitcnt lgkmcnt(0)
	s_barrier
	s_cmp_eq_u32 s61, 0
	s_cbranch_scc1 .Lgru_noflag
	v_readfirstlane_b32 s55, v248
	s_nop 3
	s_cmp_lg_u32 s55, 0
	s_cbranch_scc1 .Lgru_noflag_clear
	v_mov_b32_e32 v224, s61
	v_mov_b32_e32 v225, 1
	global_store_byte v224, v225, s[52:53] offset:11 sc0 sc1
.Lgru_noflag_clear:
	s_mov_b32 s61, 0
.Lgru_noflag:
	ds_read_b32 v5, v5
	v_lshrrev_b32_e32 v18, 16, v7
	v_mul_u32_u24_e32 v8, 0x619, v19
	v_mad_u32_u24 v7, v18, s4, v4
	v_lshrrev_b32_e32 v20, 16, v8
	v_lshlrev_b16_e32 v6, 3, v6
	v_mad_u32_u24 v4, v20, s4, v4
	ds_read_b32 v7, v7
	ds_read_b32 v21, v4
	v_lshlrev_b32_e32 v190, 1, v6
	v_mul_u32_u24_e32 v3, 0x2b0, v3
	s_mov_b32 s9, 0x15000
	v_add3_u32 v22, v3, v190, s9
	v_mul_lo_u16_e32 v3, 42, v18
	s_movk_i32 s8, 0x2a0
	v_mov_b64_e32 v[12:13], s[10:11]
	v_sub_u16_e32 v3, v51, v3
	s_waitcnt lgkmcnt(2)
	v_mad_i64_i32 v[4:5], s[4:5], v5, s8, v[12:13]
	v_mov_b32_e32 v191, 0
	v_lshlrev_b16_e32 v3, 3, v3
	v_lshl_add_u64 v[14:15], v[4:5], 0, v[190:191]
	s_waitcnt lgkmcnt(1)
	v_mad_i64_i32 v[4:5], s[4:5], v7, s8, v[12:13]
	v_lshlrev_b32_e32 v190, 1, v3
	v_lshl_add_u64 v[16:17], v[4:5], 0, v[190:191]
	v_mul_u32_u24_e32 v3, 0x2b0, v18
	global_load_dwordx4 v[4:7], v[14:15], off
	global_load_dwordx4 v[8:11], v[16:17], off
	v_add3_u32 v16, v3, v190, s9
	v_mul_lo_u16_e32 v3, 42, v20
	v_sub_u16_e32 v3, v19, v3
	v_lshlrev_b16_e32 v3, 3, v3
	s_waitcnt lgkmcnt(0)
	v_mad_i64_i32 v[12:13], s[4:5], v21, s8, v[12:13]
	v_lshlrev_b32_e32 v190, 1, v3
	v_lshl_add_u64 v[12:13], v[12:13], 0, v[190:191]
	global_load_dwordx4 v[12:15], v[12:13], off
	v_cmp_gt_u32_e32 vcc, 2, v2
	v_mul_u32_u24_e32 v17, 0x2b0, v20
	v_lshlrev_b32_e32 v192, 3, v2
	v_cndmask_b32_e64 v3, 32, 40, vcc
	v_or_b32_e32 v3, v3, v2
	v_add3_u32 v17, v17, v190, s9
	v_lshlrev_b32_e32 v190, 3, v3
	s_waitcnt vmcnt(2)
	ds_write_b128 v22, v[4:7]
	s_waitcnt vmcnt(1)
	ds_write_b128 v16, v[8:11]
	s_waitcnt vmcnt(0)
	ds_write_b128 v17, v[12:15]
	s_and_saveexec_b64 s[4:5], s[6:7]
	s_xor_b64 s[4:5], exec, s[4:5]
	v_lshlrev_b32_e32 v192, 3, v2
	v_lshlrev_b32_e32 v190, 3, v3
	v_mov_b32_e32 v193, v191
	s_or_saveexec_b64 s[4:5], s[4:5]
	v_bfe_u32 v0, v0, 3, 5
	s_xor_b64 exec, exec, s[4:5]
	s_cbranch_execz .LBB3_61
	s_movk_i32 s8, 0x64
	v_mov_b32_e32 v4, 0x25604
	v_add_u32_e32 v4, s48, v4
	v_mad_u32_u24 v4, v0, s8, v4
	ds_read_b32 v6, v4
	s_movk_i32 s8, 0x2a0
	v_mov_b64_e32 v[4:5], s[10:11]
	v_mov_b32_e32 v193, 0
	v_mov_b32_e32 v7, v193
	s_waitcnt lgkmcnt(0)
	v_mad_i64_i32 v[4:5], s[8:9], v6, s8, v[4:5]
	v_lshlrev_b32_e32 v6, 4, v2
	v_lshl_add_u64 v[6:7], v[4:5], 0, v[6:7]
	global_load_dwordx4 v[178:181], v[6:7], off
	global_load_dwordx4 v[174:177], v[6:7], off offset:128
	global_load_dwordx4 v[170:173], v[6:7], off offset:256
	global_load_dwordx4 v[166:169], v[6:7], off offset:384
	v_lshlrev_b32_e32 v2, 4, v3
	v_mov_b32_e32 v3, v193
	v_lshl_add_u64 v[2:3], v[4:5], 0, v[2:3]
	global_load_dwordx4 v[186:189], v[6:7], off offset:512
	global_load_dwordx4 v[182:185], v[2:3], off
	v_mov_b32_e32 v191, v193

.LBB3_63:
	s_cmp_eq_u32 s14, s50
	s_cbranch_scc1 .Lgru_dump
	s_and_saveexec_b64 s[0:1], s[6:7]
	s_xor_b64 s[0:1], exec, s[0:1]
	s_cbranch_execz .LBB3_66
	s_and_b32 s21, s14, 1
	s_mulk_i32 s21, 0x1e00
	v_add_u32_e32 v231, s21, v211
	ds_read_b128 v[166:169], v231
	ds_read_b128 v[170:173], v231 offset:32
	ds_read_b128 v[174:177], v231 offset:64
	ds_read_b128 v[178:181], v231 offset:96
	ds_read_b128 v[182:185], v231 offset:128
	ds_read_b128 v[186:189], v231 offset:160
	ds_read_b128 v[196:199], v231 offset:192
	ds_read_b128 v[232:235], v215
	ds_read_b128 v[236:239], v215 offset:7168
	ds_read_b128 v[240:243], v215 offset:14336
	ds_read_b128 v[244:247], v215 offset:1024
	s_cmp_lt_u32 s14, 2
	s_cbranch_scc1 .LBB3_66
	v_exp_f32_e32 v0, v2
	v_exp_f32_e32 v2, v3
	v_exp_f32_e32 v3, v4
	v_exp_f32_e32 v4, v5
	v_exp_f32_e32 v5, v6
	v_exp_f32_e32 v6, v7
	v_exp_f32_e32 v7, v8
	v_exp_f32_e32 v8, v9
	v_exp_f32_e32 v9, v10
	v_exp_f32_e32 v10, v11
	v_exp_f32_e32 v11, v12
	v_exp_f32_e32 v12, v13
	v_exp_f32_e32 v13, v14
	v_add_f32_e32 v0, 1.0, v0
	v_exp_f32_e32 v14, v18
	v_exp_f32_e32 v18, v19
	v_exp_f32_e32 v19, v20
	v_exp_f32_e32 v20, v21
	v_exp_f32_e32 v21, v22
	v_exp_f32_e32 v22, v23
	v_exp_f32_e32 v23, v24
	v_exp_f32_e32 v24, v25
	v_exp_f32_e32 v25, v26
	v_exp_f32_e32 v26, v27
	v_exp_f32_e32 v27, v28
	v_exp_f32_e32 v28, v29
	v_exp_f32_e32 v29, v30
	v_add_f32_e32 v30, 1.0, v2
	v_add_f32_e32 v65, 1.0, v11
	v_rcp_f32_e32 v2, v0
	v_add_f32_e32 v79, 1.0, v12
	v_rcp_f32_e32 v12, v65
	v_add_f32_e32 v31, 1.0, v3
	v_rcp_f32_e32 v3, v30
	v_add_f32_e32 v47, 1.0, v6
	v_add_f32_e32 v80, 1.0, v13
	v_rcp_f32_e32 v13, v79
	v_add_f32_e32 v32, 1.0, v4
	v_add_f32_e32 v48, 1.0, v7
	v_rcp_f32_e32 v4, v31
	v_rcp_f32_e32 v7, v47
	v_fma_f32 v0, v2, v34, v66
	v_add_f32_e32 v81, 1.0, v14
	v_rcp_f32_e32 v14, v80
	v_fma_f32 v66, v12, v44, v76
	v_exp_f32_e32 v0, v0
	v_add_f32_e32 v33, 1.0, v5
	v_add_f32_e32 v49, 1.0, v8
	v_rcp_f32_e32 v5, v32
	v_rcp_f32_e32 v8, v48
	v_fma_f32 v31, v3, v35, v67
	v_exp_f32_e32 v66, v66
	v_fma_f32 v67, v13, v45, v77
	v_exp_f32_e32 v31, v31
	v_rcp_f32_e32 v6, v33
	v_fma_f32 v32, v4, v36, v68
	v_fma_f32 v48, v7, v39, v71
	v_exp_f32_e32 v67, v67
	v_fma_f32 v68, v14, v46, v78
	v_exp_f32_e32 v32, v32
	v_exp_f32_e32 v48, v48
	v_add_f32_e32 v0, 1.0, v0
	v_add_f32_e32 v63, 1.0, v9
	v_rcp_f32_e32 v9, v49
	v_fma_f32 v33, v5, v37, v69
	v_fma_f32 v49, v8, v40, v72
	v_exp_f32_e32 v68, v68
	v_add_f32_e32 v76, 1.0, v66
	v_rcp_f32_e32 v66, v0
	v_exp_f32_e32 v33, v33
	v_exp_f32_e32 v49, v49
	v_add_f32_e32 v31, 1.0, v31
	v_fma_f32 v47, v6, v38, v70
	v_add_f32_e32 v77, 1.0, v67
	v_rcp_f32_e32 v67, v31
	v_add_f32_e32 v219, 1.0, v18
	v_rcp_f32_e32 v18, v81
	v_exp_f32_e32 v47, v47
	v_add_f32_e32 v32, 1.0, v32
	v_add_f32_e32 v48, 1.0, v48
	v_add_f32_e32 v78, 1.0, v68
	v_rcp_f32_e32 v68, v32
	v_rcp_f32_e32 v71, v48
	v_fma_f32 v66, v66, -2.0, 1.0
	v_add_f32_e32 v220, 1.0, v19
	v_rcp_f32_e32 v19, v219
	v_add_f32_e32 v33, 1.0, v33
	v_add_f32_e32 v49, 1.0, v49
	v_add_f32_e32 v64, 1.0, v10
	v_sub_f32_e32 v0, v50, v66
	v_rcp_f32_e32 v10, v63
	v_rcp_f32_e32 v69, v33
	v_rcp_f32_e32 v72, v49
	v_fma_f32 v67, v67, -2.0, 1.0
	v_add_f32_e32 v221, 1.0, v20
	v_rcp_f32_e32 v20, v220
	v_add_f32_e32 v47, 1.0, v47
	v_fma_f32 v50, v18, v0, v66
	v_rcp_f32_e32 v11, v64
	v_sub_f32_e32 v0, v51, v67
	v_fma_f32 v63, v9, v41, v73
	v_rcp_f32_e32 v70, v47
	v_fma_f32 v68, v68, -2.0, 1.0
	v_add_f32_e32 v222, 1.0, v21
	v_rcp_f32_e32 v21, v221
	v_exp_f32_e32 v63, v63
	v_fma_f32 v51, v19, v0, v67
	v_fma_f32 v64, v10, v42, v74
	v_sub_f32_e32 v0, v52, v68
	v_fma_f32 v69, v69, -2.0, 1.0
	v_add_f32_e32 v223, 1.0, v22
	v_rcp_f32_e32 v22, v222
	v_exp_f32_e32 v64, v64
	v_fma_f32 v52, v20, v0, v68
	v_fma_f32 v65, v11, v43, v75
	v_sub_f32_e32 v0, v53, v69
	v_fma_f32 v70, v70, -2.0, 1.0
	v_add_f32_e32 v224, 1.0, v23
	v_rcp_f32_e32 v23, v223
	v_exp_f32_e32 v65, v65
	v_add_f32_e32 v63, 1.0, v63
	v_fma_f32 v53, v21, v0, v69
	v_rcp_f32_e32 v73, v63
	v_sub_f32_e32 v0, v54, v70
	v_fma_f32 v71, v71, -2.0, 1.0
	v_add_f32_e32 v225, 1.0, v24
	v_rcp_f32_e32 v24, v224
	v_add_f32_e32 v64, 1.0, v64
	v_fma_f32 v54, v22, v0, v70
	v_rcp_f32_e32 v74, v64
	v_sub_f32_e32 v0, v55, v71
	v_fma_f32 v72, v72, -2.0, 1.0
	v_add_f32_e32 v226, 1.0, v25
	v_rcp_f32_e32 v25, v225
	v_add_f32_e32 v65, 1.0, v65
	v_fma_f32 v55, v23, v0, v71
	v_rcp_f32_e32 v75, v65
	v_sub_f32_e32 v0, v56, v72
	v_fma_f32 v73, v73, -2.0, 1.0
	v_add_f32_e32 v227, 1.0, v26
	v_rcp_f32_e32 v26, v226
	v_fma_f32 v56, v24, v0, v72
	v_rcp_f32_e32 v76, v76
	v_sub_f32_e32 v0, v57, v73
	v_fma_f32 v74, v74, -2.0, 1.0
	v_add_f32_e32 v228, 1.0, v27
	v_rcp_f32_e32 v27, v227
	v_fma_f32 v57, v25, v0, v73
	v_rcp_f32_e32 v77, v77
	v_sub_f32_e32 v0, v58, v74
	v_fma_f32 v75, v75, -2.0, 1.0
	v_add_f32_e32 v229, 1.0, v28
	v_rcp_f32_e32 v28, v228
	v_fma_f32 v58, v26, v0, v74
	v_rcp_f32_e32 v78, v78
	v_sub_f32_e32 v0, v59, v75
	v_fma_f32 v76, v76, -2.0, 1.0
	v_add_f32_e32 v230, 1.0, v29
	v_rcp_f32_e32 v29, v229
	v_fma_f32 v59, v27, v0, v75
	v_rcp_f32_e32 v30, v230
	v_sub_f32_e32 v0, v60, v76
	v_fma_f32 v77, v77, -2.0, 1.0
	v_fma_f32 v60, v28, v0, v76
	v_fma_f32 v78, v78, -2.0, 1.0
	v_sub_f32_e32 v0, v61, v77
	s_nop 0
	v_fma_f32 v61, v29, v0, v77
	v_sub_f32_e32 v0, v62, v78
	s_nop 0
	v_fma_f32 v62, v30, v0, v78
	v_cvt_pk_f16_f32 v33, v52, v53
	v_cvt_f16_f32_e32 v0, v62
	v_cvt_pk_f16_f32 v32, v50, v51
	v_cvt_pk_f16_f32 v49, v56, v57
	v_cvt_pk_f16_f32 v48, v54, v55
	ds_write2_b64 v210, v[32:33], v[48:49] offset1:2
	v_cvt_pk_f16_f32 v33, v60, v61
	v_cvt_pk_f16_f32 v32, v58, v59
	v_perm_b32 v0, v208, v0, s15
	ds_write_b64 v210, v[32:33] offset:32
	ds_write_b64 v218, v[0:1]

.Lgru_sched_split:
	s_cmp_gt_u32 s49, 2
	s_cbranch_scc1 .LBB3_86
	s_add_i32 s44, s60, 0x100
	s_lshl_b32 s44, s44, 5
	s_cmp_eq_u32 s49, 2
	s_cbranch_scc1 .Lgru_sched_j2
	s_cmp_ge_u32 s60, s51
	s_cbranch_scc1 .Lgru_next_tile
	s_add_i32 s44, s60, 0x200
	s_lshl_b32 s44, s44, 5
	s_mov_b32 s47, 1
	s_movk_i32 s50, 16
	s_mov_b32 s54, s60
	s_branch .Lgru_next_tile
.Lgru_sched_j2:
	s_cmp_lt_u32 s60, s51
	s_cbranch_scc1 .Lgru_next_tile
	s_lshl_b32 s55, s51, 1
	s_cmp_ge_u32 s60, s55
	s_cbranch_scc1 .LBB3_86
	s_sub_i32 s54, s60, s51
	s_add_i32 s44, s54, 0x200
	s_lshl_b32 s44, s44, 5
	s_mov_b32 s47, 2
	s_movk_i32 s48, 64

.Lgru_dump_r3:
	v_add_u32_e32 v220, 0x400, v248
	v_min_u32_e32 v220, 0x59f, v220
	v_lshlrev_b32_e32 v220, 4, v220
	v_add_u32_e32 v221, 0x1fc00, v219
	v_add_u32_e32 v222, 0x1fc00, v220
	ds_read_b128 v[224:227], v221
	ds_read_b128 v[228:231], v221 offset:8192
	ds_read_b128 v[232:235], v222
	v_add_u32_e32 v221, 0x18000, v219
	v_add_u32_e32 v222, 0x1a000, v219
	v_add_u32_e32 v223, 0x18000, v220
	s_waitcnt lgkmcnt(2)
	global_store_dwordx4 v221, v[224:227], s[58:59] sc0 sc1
	s_waitcnt lgkmcnt(1)
	global_store_dwordx4 v222, v[228:231], s[58:59] sc0 sc1
	s_waitcnt lgkmcnt(0)
	global_store_dwordx4 v223, v[232:235], s[58:59] sc0 sc1
	s_add_i32 s61, s54, 1
	s_branch .Lgru_tile_end

.Lgru_rs_r3:
	v_add_u32_e32 v220, 0x400, v248
	v_min_u32_e32 v220, 0x59f, v220
	v_lshlrev_b32_e32 v220, 4, v220
	v_add_u32_e32 v221, 0x18000, v219
	v_add_u32_e32 v222, 0x1a000, v219
	v_add_u32_e32 v223, 0x18000, v220
	global_load_dwordx4 v[224:227], v221, s[58:59] sc0 sc1
	global_load_dwordx4 v[228:231], v222, s[58:59] sc0 sc1
	global_load_dwordx4 v[232:235], v223, s[58:59] sc0 sc1
	v_add_u32_e32 v221, 0x1fc00, v219
	v_add_u32_e32 v222, 0x1fc00, v220
	s_waitcnt vmcnt(2)
	ds_write_b128 v221, v[224:227]
	s_waitcnt vmcnt(1)
	ds_write_b128 v221, v[228:231] offset:8192
	s_waitcnt vmcnt(0)
	ds_write_b128 v222, v[232:235]
	s_movk_i32 s14, 16
	s_waitcnt lgkmcnt(0)
	s_barrier
	s_branch .LBB3_63
